# dense loop: per-tile row max replaced by a check of the f32 row sum (<=400 implies every p fits e4m3) before the e4m3 packing; rare exact power-of-two rescale from the probabilities
# speedup vs baseline: 1.0211x; 1.0104x over previous
.LBB0_409:
	s_waitcnt vmcnt(0)
	v_mov_b32_e32 v254, v116
	v_mov_b32_e32 v255, v118
	ds_write_b64 v189, v[254:255] offset:8192
	v_mov_b32_e32 v244, v117
	v_mov_b32_e32 v245, v119
	ds_write_b64 v190, v[244:245] offset:8192
	ds_write_b128 v191, v[120:123] offset:40960
	ds_read_b128 v[68:71], v192 offset:49152
	ds_read_b128 v[72:75], v193 offset:49152
	ds_read_b128 v[208:211], v194 offset:49152
	ds_read_b128 v[212:215], v195 offset:49152
	ds_read_b128 v[200:203], v192 offset:53248
	ds_read_b128 v[204:207], v193 offset:53248
	v_add_f32_e32 v241, v154, v155
	v_add_f32_e32 v240, v173, v177
	v_add_f32_e32 v241, v130, v241
	v_add_f32_e32 v240, v165, v240
	v_add_f32_e32 v241, v131, v241
	v_add_f32_e32 v240, v166, v240
	v_add_f32_e32 v241, v128, v241
	s_waitcnt lgkmcnt(4)
	v_mfma_scale_f32_32x32x64_f8f6f4 v[84:99], v[68:75], v[100:107], v[216:231], v188, v247 op_sel_hi:[0,0,0]
	v_add_f32_e32 v240, v174, v240
	v_add_f32_e32 v241, v129, v241
	v_add_f32_e32 v240, v178, v240
	v_add_f32_e32 v241, v126, v241
	v_add_f32_e32 v240, v167, v240
	v_add_f32_e32 v241, v127, v241
	v_add_f32_e32 v240, v168, v240
	s_waitcnt lgkmcnt(2)
	v_mfma_scale_f32_32x32x64_f8f6f4 v[84:99], v[208:215], v[108:115], v[84:99], v188, v247 op_sel_hi:[0,0,0]
	v_add_f32_e32 v241, v124, v241
	v_add_f32_e32 v240, v175, v240
	v_add_f32_e32 v241, v125, v241
	v_add_f32_e32 v240, v179, v240
	v_add_f32_e32 v241, v160, v241
	v_add_f32_e32 v240, v169, v240
	v_add_f32_e32 v241, v161, v241
	s_waitcnt lgkmcnt(0)
	v_mfma_scale_f32_32x32x64_f8f6f4 v[68:83], v[200:207], v[100:107], v[216:231], v188, v247 op_sel_hi:[0,0,0]
	ds_read_b128 v[200:203], v194 offset:53248
	ds_read_b128 v[204:207], v195 offset:53248
	v_add_f32_e32 v240, v170, v240
	v_add_f32_e32 v241, v158, v241
	v_add_f32_e32 v240, v176, v240
	v_add_f32_e32 v241, v159, v241
	v_add_f32_e32 v240, v180, v240
	v_add_f32_e32 v241, v156, v241
	v_add_f32_e32 v240, v171, v240
	v_add_f32_e32 v241, v157, v241
	s_waitcnt lgkmcnt(0)
	v_mfma_scale_f32_32x32x64_f8f6f4 v[68:83], v[200:207], v[108:115], v[68:83], v188, v247 op_sel_hi:[0,0,0]
	v_add_f32_e32 v240, v172, v240
	v_add_f32_e32 v162, v240, v241
	v_mov_b32_e32 v163, v162
	s_nop 0
	s_nop 0
	v_permlane32_swap_b32_e32 v162, v163
	v_add_f32_e32 v162, v162, v163
	v_cmp_ge_f32_e32 vcc, 0x43c80000, v162
	s_cmp_eq_u64 vcc, exec
	s_cbranch_scc1 .Lring_norare_a0
	s_nop 15
	s_nop 15
	v_max3_f32 v240, v173, v177, v165
	v_max3_f32 v240, v240, v166, v174
	v_max3_f32 v240, v240, v178, v167
	v_max3_f32 v240, v240, v168, v175
	v_max3_f32 v240, v240, v179, v169
	v_max3_f32 v240, v240, v170, v176
	v_max3_f32 v240, v240, v180, v171
	v_max3_f32 v240, v240, v172, v154
	v_max3_f32 v240, v240, v155, v130
	v_max3_f32 v240, v240, v131, v128
	v_max3_f32 v240, v240, v129, v126
	v_max3_f32 v240, v240, v127, v124
	v_max3_f32 v240, v240, v125, v160
	v_max3_f32 v240, v240, v161, v158
	v_max3_f32 v240, v240, v159, v156
	v_max_f32_e32 v240, v240, v157
	v_mov_b32_e32 v241, v240
	s_nop 1
	v_permlane32_swap_b32_e32 v240, v241
	v_max_f32_e32 v240, v240, v241
	v_log_f32_e32 v249, v240
	s_nop 0
	v_ceil_f32_e32 v249, v249
	v_max_f32_e32 v249, 0, v249
	v_exp_f32_e64 v252, -v249
	s_nop 0
	v_fmamk_f32 v153, v249, 0x41000000, v153
	v_mul_f32_e32 v173, v173, v252
	v_mul_f32_e32 v177, v177, v252
	v_mul_f32_e32 v165, v165, v252
	v_mul_f32_e32 v166, v166, v252
	v_mul_f32_e32 v174, v174, v252
	v_mul_f32_e32 v178, v178, v252
	v_mul_f32_e32 v167, v167, v252
	v_mul_f32_e32 v168, v168, v252
	v_mul_f32_e32 v175, v175, v252
	v_mul_f32_e32 v179, v179, v252
	v_mul_f32_e32 v169, v169, v252
	v_mul_f32_e32 v170, v170, v252
	v_mul_f32_e32 v176, v176, v252
	v_mul_f32_e32 v180, v180, v252
	v_mul_f32_e32 v171, v171, v252
	v_mul_f32_e32 v172, v172, v252
	v_mul_f32_e32 v154, v154, v252
	v_mul_f32_e32 v155, v155, v252
	v_mul_f32_e32 v130, v130, v252
	v_mul_f32_e32 v131, v131, v252
	v_mul_f32_e32 v128, v128, v252
	v_mul_f32_e32 v129, v129, v252
	v_mul_f32_e32 v126, v126, v252
	v_mul_f32_e32 v127, v127, v252
	v_mul_f32_e32 v124, v124, v252
	v_mul_f32_e32 v125, v125, v252
	v_mul_f32_e32 v160, v160, v252
	v_mul_f32_e32 v161, v161, v252
	v_mul_f32_e32 v158, v158, v252
	v_mul_f32_e32 v159, v159, v252
	v_mul_f32_e32 v156, v156, v252
	v_mul_f32_e32 v157, v157, v252
	v_mul_f32_e32 v162, v162, v252
	v_mul_f32_e32 v145, v145, v252
	v_sub_f32_e32 v84, v84, v249
	v_sub_f32_e32 v85, v85, v249
	v_sub_f32_e32 v86, v86, v249
	v_sub_f32_e32 v87, v87, v249
	v_sub_f32_e32 v88, v88, v249
	v_sub_f32_e32 v89, v89, v249
	v_sub_f32_e32 v90, v90, v249
	v_sub_f32_e32 v91, v91, v249
	v_sub_f32_e32 v92, v92, v249
	v_sub_f32_e32 v93, v93, v249
	v_sub_f32_e32 v94, v94, v249
	v_sub_f32_e32 v95, v95, v249
	v_sub_f32_e32 v96, v96, v249
	v_sub_f32_e32 v97, v97, v249
	v_sub_f32_e32 v98, v98, v249
	v_sub_f32_e32 v99, v99, v249
	v_sub_f32_e32 v68, v68, v249
	v_sub_f32_e32 v69, v69, v249
	v_sub_f32_e32 v70, v70, v249
	v_sub_f32_e32 v71, v71, v249
	v_sub_f32_e32 v72, v72, v249
	v_sub_f32_e32 v73, v73, v249
	v_sub_f32_e32 v74, v74, v249
	v_sub_f32_e32 v75, v75, v249
	v_sub_f32_e32 v76, v76, v249
	v_sub_f32_e32 v77, v77, v249
	v_sub_f32_e32 v78, v78, v249
	v_sub_f32_e32 v79, v79, v249
	v_sub_f32_e32 v80, v80, v249
	v_sub_f32_e32 v81, v81, v249
	v_sub_f32_e32 v82, v82, v249
	v_sub_f32_e32 v83, v83, v249
	v_sub_f32_e32 v216, v216, v249
	v_sub_f32_e32 v217, v217, v249
	v_sub_f32_e32 v218, v218, v249
	v_sub_f32_e32 v219, v219, v249
	v_sub_f32_e32 v220, v220, v249
	v_sub_f32_e32 v221, v221, v249
	v_sub_f32_e32 v222, v222, v249
	v_sub_f32_e32 v223, v223, v249
	v_sub_f32_e32 v224, v224, v249
	v_sub_f32_e32 v225, v225, v249
	v_sub_f32_e32 v226, v226, v249
	v_sub_f32_e32 v227, v227, v249
	v_sub_f32_e32 v228, v228, v249
	v_sub_f32_e32 v229, v229, v249
	v_sub_f32_e32 v230, v230, v249
	v_sub_f32_e32 v231, v231, v249
	s_and_saveexec_b64 s[8:9], s[6:7]
	ds_write_b32 v184, v252 offset:128
	s_or_b64 exec, exec, s[8:9]
	s_waitcnt lgkmcnt(0)
	v_add_u32_e32 v253, v135, v185
	ds_read_b128 v[212:215], v253 offset:224
	ds_read_b128 v[208:211], v253 offset:192
	ds_read_b128 v[204:207], v253 offset:160
	ds_read_b128 v[200:203], v253 offset:128
	s_waitcnt lgkmcnt(0)
	v_pk_mul_f32 v[52:53], v[52:53], v[200:201]
	v_pk_mul_f32 v[54:55], v[54:55], v[202:203]
	v_pk_mul_f32 v[56:57], v[56:57], v[204:205]
	v_pk_mul_f32 v[58:59], v[58:59], v[206:207]
	v_pk_mul_f32 v[60:61], v[60:61], v[208:209]
	v_pk_mul_f32 v[62:63], v[62:63], v[210:211]
	v_pk_mul_f32 v[64:65], v[64:65], v[212:213]
	v_pk_mul_f32 v[66:67], v[66:67], v[214:215]
	v_pk_mul_f32 v[36:37], v[36:37], v[200:201]
	v_pk_mul_f32 v[38:39], v[38:39], v[202:203]
	v_pk_mul_f32 v[40:41], v[40:41], v[204:205]
	v_pk_mul_f32 v[42:43], v[42:43], v[206:207]
	v_pk_mul_f32 v[44:45], v[44:45], v[208:209]
	v_pk_mul_f32 v[46:47], v[46:47], v[210:211]
	v_pk_mul_f32 v[48:49], v[48:49], v[212:213]
	v_pk_mul_f32 v[50:51], v[50:51], v[214:215]
	v_pk_mul_f32 v[20:21], v[20:21], v[200:201]
	v_pk_mul_f32 v[22:23], v[22:23], v[202:203]
	v_pk_mul_f32 v[24:25], v[24:25], v[204:205]
	v_pk_mul_f32 v[26:27], v[26:27], v[206:207]
	v_pk_mul_f32 v[28:29], v[28:29], v[208:209]
	v_pk_mul_f32 v[30:31], v[30:31], v[210:211]
	v_pk_mul_f32 v[32:33], v[32:33], v[212:213]
	v_pk_mul_f32 v[34:35], v[34:35], v[214:215]
	v_pk_mul_f32 v[4:5], v[4:5], v[200:201]
	v_pk_mul_f32 v[6:7], v[6:7], v[202:203]
	v_pk_mul_f32 v[8:9], v[8:9], v[204:205]
	v_pk_mul_f32 v[10:11], v[10:11], v[206:207]
	v_pk_mul_f32 v[12:13], v[12:13], v[208:209]
	v_pk_mul_f32 v[14:15], v[14:15], v[210:211]
	v_pk_mul_f32 v[16:17], v[16:17], v[212:213]
	v_pk_mul_f32 v[18:19], v[18:19], v[214:215]
.Lring_norare_a0:
	ds_read_b128 v[200:203], v197
	ds_read_b128 v[204:207], v198
	ds_read_b128 v[208:211], v197 offset:2048
	ds_read_b128 v[212:215], v198 offset:2048
	v_add_u32_e32 v252, 0xffffe000, v152
	v_mov_b32_e32 v253, v3
	v_lshl_add_u64 v[252:253], v[148:149], 0, v[252:253]
	v_add_f32_e32 v145, v145, v162
	v_cvt_pk_fp8_f32 v232, v173, v177
	v_cvt_pk_fp8_f32 v233, v174, v178
	v_cvt_pk_fp8_f32 v234, v175, v179
	v_cvt_pk_fp8_f32 v235, v176, v180
	v_cvt_pk_fp8_f32 v232, v165, v166 op_sel:[0,0,1]
	v_cvt_pk_fp8_f32 v233, v167, v168 op_sel:[0,0,1]
	v_cvt_pk_fp8_f32 v234, v169, v170 op_sel:[0,0,1]
	v_cvt_pk_fp8_f32 v235, v171, v172 op_sel:[0,0,1]
	v_cvt_pk_fp8_f32 v236, v154, v155
	v_cvt_pk_fp8_f32 v237, v128, v129
	v_cvt_pk_fp8_f32 v238, v124, v125
	v_cvt_pk_fp8_f32 v239, v158, v159
	v_cvt_pk_fp8_f32 v236, v130, v131 op_sel:[0,0,1]
	v_cvt_pk_fp8_f32 v237, v126, v127 op_sel:[0,0,1]
	global_load_dwordx4 v[124:127], v[150:151], off offset:-64
	global_load_dwordx4 v[128:131], v[252:253], off
	s_waitcnt lgkmcnt(2)
	v_cvt_pk_fp8_f32 v238, v160, v161 op_sel:[0,0,1]
	v_cvt_pk_fp8_f32 v239, v156, v157 op_sel:[0,0,1]
	s_nop 0
	s_nop 0
	v_mfma_scale_f32_32x32x64_f8f6f4 v[52:67], v[232:239], v[200:207], v[52:67], v188, v188 op_sel_hi:[0,0,0]
	v_exp_f32_e32 v165, v84
	v_exp_f32_e32 v169, v85
	v_exp_f32_e32 v2, v86
	v_exp_f32_e32 v155, v87
	v_exp_f32_e32 v166, v88
	v_exp_f32_e32 v170, v89
	v_exp_f32_e32 v156, v90
	v_exp_f32_e32 v157, v91
	s_waitcnt lgkmcnt(0)
	v_mfma_scale_f32_32x32x64_f8f6f4 v[36:51], v[232:239], v[208:215], v[36:51], v188, v188 op_sel_hi:[0,0,0]
	ds_read_b128 v[200:203], v197 offset:4096
	ds_read_b128 v[204:207], v198 offset:4096
	ds_read_b128 v[208:211], v197 offset:6144
	ds_read_b128 v[212:215], v198 offset:6144
	v_exp_f32_e32 v167, v92
	v_exp_f32_e32 v171, v93
	v_exp_f32_e32 v158, v94
	v_exp_f32_e32 v159, v95
	v_exp_f32_e32 v168, v96
	v_exp_f32_e32 v172, v97
	v_exp_f32_e32 v160, v98
	v_exp_f32_e32 v161, v99
	s_waitcnt lgkmcnt(2)
	v_mfma_scale_f32_32x32x64_f8f6f4 v[20:35], v[232:239], v[200:207], v[20:35], v188, v188 op_sel_hi:[0,0,0]
	v_exp_f32_e32 v173, v68
	v_exp_f32_e32 v174, v69
	v_exp_f32_e32 v175, v70
	v_exp_f32_e32 v176, v71
	v_exp_f32_e32 v177, v72
	v_exp_f32_e32 v178, v73
	v_exp_f32_e32 v179, v74
	v_exp_f32_e32 v180, v75
	s_waitcnt lgkmcnt(0)
	v_mfma_scale_f32_32x32x64_f8f6f4 v[4:19], v[232:239], v[208:215], v[4:19], v188, v188 op_sel_hi:[0,0,0]
	v_exp_f32_e32 v181, v76
	v_exp_f32_e32 v182, v77
	v_exp_f32_e32 v183, v78
	v_exp_f32_e32 v246, v79
	v_exp_f32_e32 v248, v80
	v_exp_f32_e32 v250, v81
	v_exp_f32_e32 v251, v82
	v_exp_f32_e32 v164, v83
	s_waitcnt lgkmcnt(0)
	s_barrier
	s_waitcnt vmcnt(0)
	v_mov_b32_e32 v254, v124
	v_mov_b32_e32 v255, v126
	ds_write_b64 v189, v[254:255] offset:24576
	v_mov_b32_e32 v244, v125
	v_mov_b32_e32 v245, v127
	ds_write_b64 v190, v[244:245] offset:24576
	ds_write_b128 v191, v[128:131] offset:57344
	s_cmp_gt_u32 s15, 60
	s_cselect_b64 s[8:9], -1, 0
	s_and_b64 vcc, exec, s[8:9]
	s_cbranch_vccnz .Lring_noload_b0
	v_mov_b32_e32 v252, v152
	v_mov_b32_e32 v253, v3
	v_lshl_add_u64 v[120:121], v[148:149], 0, v[252:253]
	global_load_dwordx4 v[116:119], v[150:151], off
	s_nop 0
	global_load_dwordx4 v[120:123], v[120:121], off
.Lring_noload_b0:
	ds_read_b128 v[68:71], v192 offset:40960
	ds_read_b128 v[72:75], v193 offset:40960
	ds_read_b128 v[208:211], v194 offset:40960
	ds_read_b128 v[212:215], v195 offset:40960
	ds_read_b128 v[200:203], v192 offset:45056
	ds_read_b128 v[204:207], v193 offset:45056
	v_add_f32_e32 v241, v173, v174
	v_add_f32_e32 v240, v165, v169
	v_add_f32_e32 v241, v175, v241
	v_add_f32_e32 v240, v2, v240
	v_add_f32_e32 v241, v176, v241
	v_add_f32_e32 v240, v155, v240
	v_add_f32_e32 v241, v177, v241
	s_waitcnt lgkmcnt(4)
	v_mfma_scale_f32_32x32x64_f8f6f4 v[84:99], v[68:75], v[100:107], v[216:231], v188, v247 op_sel_hi:[0,0,0]
	v_add_f32_e32 v240, v166, v240
	v_add_f32_e32 v241, v178, v241
	v_add_f32_e32 v240, v170, v240
	v_add_f32_e32 v241, v179, v241
	v_add_f32_e32 v240, v156, v240
	v_add_f32_e32 v241, v180, v241
	v_add_f32_e32 v240, v157, v240
	s_waitcnt lgkmcnt(2)
	v_mfma_scale_f32_32x32x64_f8f6f4 v[84:99], v[208:215], v[108:115], v[84:99], v188, v247 op_sel_hi:[0,0,0]
	v_add_f32_e32 v241, v181, v241
	v_add_f32_e32 v240, v167, v240
	v_add_f32_e32 v241, v182, v241
	v_add_f32_e32 v240, v171, v240
	v_add_f32_e32 v241, v183, v241
	v_add_f32_e32 v240, v158, v240
	v_add_f32_e32 v241, v246, v241
	s_waitcnt lgkmcnt(0)
	v_mfma_scale_f32_32x32x64_f8f6f4 v[68:83], v[200:207], v[100:107], v[216:231], v188, v247 op_sel_hi:[0,0,0]
	ds_read_b128 v[200:203], v194 offset:45056
	ds_read_b128 v[204:207], v195 offset:45056
	v_add_f32_e32 v240, v159, v240
	v_add_f32_e32 v241, v248, v241
	v_add_f32_e32 v240, v168, v240
	v_add_f32_e32 v241, v250, v241
	v_add_f32_e32 v240, v172, v240
	v_add_f32_e32 v241, v251, v241
	v_add_f32_e32 v240, v160, v240
	v_add_f32_e32 v241, v164, v241
	s_waitcnt lgkmcnt(0)
	v_mfma_scale_f32_32x32x64_f8f6f4 v[68:83], v[200:207], v[108:115], v[68:83], v188, v247 op_sel_hi:[0,0,0]
	v_add_f32_e32 v240, v161, v240
	v_add_f32_e32 v162, v240, v241
	v_mov_b32_e32 v163, v162
	s_nop 0
	s_nop 0
	v_permlane32_swap_b32_e32 v162, v163
	v_add_f32_e32 v162, v162, v163
	v_cmp_ge_f32_e32 vcc, 0x43c80000, v162
	s_cmp_eq_u64 vcc, exec
	s_cbranch_scc1 .Lring_norare_b0
	s_nop 15
	s_nop 15
	v_max3_f32 v240, v165, v169, v2
	v_max3_f32 v240, v240, v155, v166
	v_max3_f32 v240, v240, v170, v156
	v_max3_f32 v240, v240, v157, v167
	v_max3_f32 v240, v240, v171, v158
	v_max3_f32 v240, v240, v159, v168
	v_max3_f32 v240, v240, v172, v160
	v_max3_f32 v240, v240, v161, v173
	v_max3_f32 v240, v240, v174, v175
	v_max3_f32 v240, v240, v176, v177
	v_max3_f32 v240, v240, v178, v179
	v_max3_f32 v240, v240, v180, v181
	v_max3_f32 v240, v240, v182, v183
	v_max3_f32 v240, v240, v246, v248
	v_max3_f32 v240, v240, v250, v251
	v_max_f32_e32 v240, v240, v164
	v_mov_b32_e32 v241, v240
	s_nop 1
	v_permlane32_swap_b32_e32 v240, v241
	v_max_f32_e32 v240, v240, v241
	v_log_f32_e32 v249, v240
	s_nop 0
	v_ceil_f32_e32 v249, v249
	v_max_f32_e32 v249, 0, v249
	v_exp_f32_e64 v252, -v249
	s_nop 0
	v_fmamk_f32 v153, v249, 0x41000000, v153
	v_mul_f32_e32 v165, v165, v252
	v_mul_f32_e32 v169, v169, v252
	v_mul_f32_e32 v2, v2, v252
	v_mul_f32_e32 v155, v155, v252
	v_mul_f32_e32 v166, v166, v252
	v_mul_f32_e32 v170, v170, v252
	v_mul_f32_e32 v156, v156, v252
	v_mul_f32_e32 v157, v157, v252
	v_mul_f32_e32 v167, v167, v252
	v_mul_f32_e32 v171, v171, v252
	v_mul_f32_e32 v158, v158, v252
	v_mul_f32_e32 v159, v159, v252
	v_mul_f32_e32 v168, v168, v252
	v_mul_f32_e32 v172, v172, v252
	v_mul_f32_e32 v160, v160, v252
	v_mul_f32_e32 v161, v161, v252
	v_mul_f32_e32 v173, v173, v252
	v_mul_f32_e32 v174, v174, v252
	v_mul_f32_e32 v175, v175, v252
	v_mul_f32_e32 v176, v176, v252
	v_mul_f32_e32 v177, v177, v252
	v_mul_f32_e32 v178, v178, v252
	v_mul_f32_e32 v179, v179, v252
	v_mul_f32_e32 v180, v180, v252
	v_mul_f32_e32 v181, v181, v252
	v_mul_f32_e32 v182, v182, v252
	v_mul_f32_e32 v183, v183, v252
	v_mul_f32_e32 v246, v246, v252
	v_mul_f32_e32 v248, v248, v252
	v_mul_f32_e32 v250, v250, v252
	v_mul_f32_e32 v251, v251, v252
	v_mul_f32_e32 v164, v164, v252
	v_mul_f32_e32 v162, v162, v252
	v_mul_f32_e32 v145, v145, v252
	v_sub_f32_e32 v84, v84, v249
	v_sub_f32_e32 v85, v85, v249
	v_sub_f32_e32 v86, v86, v249
	v_sub_f32_e32 v87, v87, v249
	v_sub_f32_e32 v88, v88, v249
	v_sub_f32_e32 v89, v89, v249
	v_sub_f32_e32 v90, v90, v249
	v_sub_f32_e32 v91, v91, v249
	v_sub_f32_e32 v92, v92, v249
	v_sub_f32_e32 v93, v93, v249
	v_sub_f32_e32 v94, v94, v249
	v_sub_f32_e32 v95, v95, v249
	v_sub_f32_e32 v96, v96, v249
	v_sub_f32_e32 v97, v97, v249
	v_sub_f32_e32 v98, v98, v249
	v_sub_f32_e32 v99, v99, v249
	v_sub_f32_e32 v68, v68, v249
	v_sub_f32_e32 v69, v69, v249
	v_sub_f32_e32 v70, v70, v249
	v_sub_f32_e32 v71, v71, v249
	v_sub_f32_e32 v72, v72, v249
	v_sub_f32_e32 v73, v73, v249
	v_sub_f32_e32 v74, v74, v249
	v_sub_f32_e32 v75, v75, v249
	v_sub_f32_e32 v76, v76, v249
	v_sub_f32_e32 v77, v77, v249
	v_sub_f32_e32 v78, v78, v249
	v_sub_f32_e32 v79, v79, v249
	v_sub_f32_e32 v80, v80, v249
	v_sub_f32_e32 v81, v81, v249
	v_sub_f32_e32 v82, v82, v249
	v_sub_f32_e32 v83, v83, v249
	v_sub_f32_e32 v216, v216, v249
	v_sub_f32_e32 v217, v217, v249
	v_sub_f32_e32 v218, v218, v249
	v_sub_f32_e32 v219, v219, v249
	v_sub_f32_e32 v220, v220, v249
	v_sub_f32_e32 v221, v221, v249
	v_sub_f32_e32 v222, v222, v249
	v_sub_f32_e32 v223, v223, v249
	v_sub_f32_e32 v224, v224, v249
	v_sub_f32_e32 v225, v225, v249
	v_sub_f32_e32 v226, v226, v249
	v_sub_f32_e32 v227, v227, v249
	v_sub_f32_e32 v228, v228, v249
	v_sub_f32_e32 v229, v229, v249
	v_sub_f32_e32 v230, v230, v249
	v_sub_f32_e32 v231, v231, v249
	s_and_saveexec_b64 s[10:11], s[6:7]
	ds_write_b32 v184, v252 offset:128
	s_or_b64 exec, exec, s[10:11]
	s_waitcnt lgkmcnt(0)
	v_add_u32_e32 v253, v135, v185
	ds_read_b128 v[212:215], v253 offset:224
	ds_read_b128 v[208:211], v253 offset:192
	ds_read_b128 v[204:207], v253 offset:160
	ds_read_b128 v[200:203], v253 offset:128
	s_waitcnt lgkmcnt(0)
	v_pk_mul_f32 v[52:53], v[52:53], v[200:201]
	v_pk_mul_f32 v[54:55], v[54:55], v[202:203]
	v_pk_mul_f32 v[56:57], v[56:57], v[204:205]
	v_pk_mul_f32 v[58:59], v[58:59], v[206:207]
	v_pk_mul_f32 v[60:61], v[60:61], v[208:209]
	v_pk_mul_f32 v[62:63], v[62:63], v[210:211]
	v_pk_mul_f32 v[64:65], v[64:65], v[212:213]
	v_pk_mul_f32 v[66:67], v[66:67], v[214:215]
	v_pk_mul_f32 v[36:37], v[36:37], v[200:201]
	v_pk_mul_f32 v[38:39], v[38:39], v[202:203]
	v_pk_mul_f32 v[40:41], v[40:41], v[204:205]
	v_pk_mul_f32 v[42:43], v[42:43], v[206:207]
	v_pk_mul_f32 v[44:45], v[44:45], v[208:209]
	v_pk_mul_f32 v[46:47], v[46:47], v[210:211]
	v_pk_mul_f32 v[48:49], v[48:49], v[212:213]
	v_pk_mul_f32 v[50:51], v[50:51], v[214:215]
	v_pk_mul_f32 v[20:21], v[20:21], v[200:201]
	v_pk_mul_f32 v[22:23], v[22:23], v[202:203]
	v_pk_mul_f32 v[24:25], v[24:25], v[204:205]
	v_pk_mul_f32 v[26:27], v[26:27], v[206:207]
	v_pk_mul_f32 v[28:29], v[28:29], v[208:209]
	v_pk_mul_f32 v[30:31], v[30:31], v[210:211]
	v_pk_mul_f32 v[32:33], v[32:33], v[212:213]
	v_pk_mul_f32 v[34:35], v[34:35], v[214:215]
	v_pk_mul_f32 v[4:5], v[4:5], v[200:201]
	v_pk_mul_f32 v[6:7], v[6:7], v[202:203]
	v_pk_mul_f32 v[8:9], v[8:9], v[204:205]
	v_pk_mul_f32 v[10:11], v[10:11], v[206:207]
	v_pk_mul_f32 v[12:13], v[12:13], v[208:209]
	v_pk_mul_f32 v[14:15], v[14:15], v[210:211]
	v_pk_mul_f32 v[16:17], v[16:17], v[212:213]
	v_pk_mul_f32 v[18:19], v[18:19], v[214:215]
.Lring_norare_b0:
	ds_read_b128 v[200:203], v197 offset:16384
	ds_read_b128 v[204:207], v198 offset:16384
	ds_read_b128 v[208:211], v197 offset:18432
	ds_read_b128 v[212:215], v198 offset:18432
	v_add_f32_e32 v145, v145, v162
	v_cvt_pk_fp8_f32 v232, v165, v169
	v_cvt_pk_fp8_f32 v233, v166, v170
	v_cvt_pk_fp8_f32 v234, v167, v171
	v_cvt_pk_fp8_f32 v235, v168, v172
	v_cvt_pk_fp8_f32 v232, v2, v155 op_sel:[0,0,1]
	v_cvt_pk_fp8_f32 v233, v156, v157 op_sel:[0,0,1]
	v_cvt_pk_fp8_f32 v234, v158, v159 op_sel:[0,0,1]
	v_cvt_pk_fp8_f32 v235, v160, v161 op_sel:[0,0,1]
	v_cvt_pk_fp8_f32 v236, v173, v174
	s_waitcnt lgkmcnt(2)
	v_cvt_pk_fp8_f32 v237, v177, v178
	v_cvt_pk_fp8_f32 v238, v181, v182
	v_cvt_pk_fp8_f32 v239, v248, v250
	v_cvt_pk_fp8_f32 v236, v175, v176 op_sel:[0,0,1]
	v_cvt_pk_fp8_f32 v237, v179, v180 op_sel:[0,0,1]
	v_cvt_pk_fp8_f32 v238, v183, v246 op_sel:[0,0,1]
	v_cvt_pk_fp8_f32 v239, v251, v164 op_sel:[0,0,1]
	s_nop 0
	s_nop 0
	v_mfma_scale_f32_32x32x64_f8f6f4 v[52:67], v[232:239], v[200:207], v[52:67], v188, v188 op_sel_hi:[0,0,0]
	v_exp_f32_e32 v173, v84
	v_exp_f32_e32 v177, v85
	v_exp_f32_e32 v165, v86
	v_exp_f32_e32 v166, v87
	v_exp_f32_e32 v174, v88
	v_exp_f32_e32 v178, v89
	v_exp_f32_e32 v167, v90
	v_exp_f32_e32 v168, v91
	s_waitcnt lgkmcnt(0)
	v_mfma_scale_f32_32x32x64_f8f6f4 v[36:51], v[232:239], v[208:215], v[36:51], v188, v188 op_sel_hi:[0,0,0]
	ds_read_b128 v[200:203], v197 offset:20480
	ds_read_b128 v[204:207], v198 offset:20480
	ds_read_b128 v[208:211], v197 offset:22528
	ds_read_b128 v[212:215], v198 offset:22528
	v_exp_f32_e32 v175, v92
	v_exp_f32_e32 v179, v93
	v_exp_f32_e32 v169, v94
	v_exp_f32_e32 v170, v95
	v_exp_f32_e32 v176, v96
	v_exp_f32_e32 v180, v97
	v_exp_f32_e32 v171, v98
	v_exp_f32_e32 v172, v99
	s_waitcnt lgkmcnt(2)
	v_mfma_scale_f32_32x32x64_f8f6f4 v[20:35], v[232:239], v[200:207], v[20:35], v188, v188 op_sel_hi:[0,0,0]
	v_exp_f32_e32 v154, v68
	v_exp_f32_e32 v155, v69
	v_exp_f32_e32 v130, v70
	v_exp_f32_e32 v131, v71
	v_exp_f32_e32 v128, v72
	v_exp_f32_e32 v129, v73
	v_exp_f32_e32 v126, v74
	v_exp_f32_e32 v127, v75
	s_waitcnt lgkmcnt(0)
	v_mfma_scale_f32_32x32x64_f8f6f4 v[4:19], v[232:239], v[208:215], v[4:19], v188, v188 op_sel_hi:[0,0,0]
	v_exp_f32_e32 v124, v76
	v_exp_f32_e32 v125, v77
	v_exp_f32_e32 v160, v78
	v_exp_f32_e32 v161, v79
	v_exp_f32_e32 v158, v80
	v_exp_f32_e32 v159, v81
	v_exp_f32_e32 v156, v82
	v_exp_f32_e32 v157, v83
	s_add_i32 s15, s15, 2
	v_lshl_add_u64 v[150:151], v[150:151], 0, s[28:29]
	v_add_u32_e32 v152, 0x4000, v152
	s_and_b64 vcc, exec, s[8:9]
	s_waitcnt lgkmcnt(0)
	s_barrier
	s_cbranch_vccnz .LBB0_421
	s_waitcnt vmcnt(0)
	v_mov_b32_e32 v254, v116
	v_mov_b32_e32 v255, v118
	ds_write_b64 v189, v[254:255]
	v_mov_b32_e32 v244, v117
	v_mov_b32_e32 v245, v119
	ds_write_b64 v190, v[244:245]
	ds_write_b128 v191, v[120:123] offset:32768
	ds_read_b128 v[68:71], v192 offset:57344
	ds_read_b128 v[72:75], v193 offset:57344
	ds_read_b128 v[208:211], v194 offset:57344
	ds_read_b128 v[212:215], v195 offset:57344
	ds_read_b128 v[200:203], v192 offset:61440
	ds_read_b128 v[204:207], v193 offset:61440
	v_add_f32_e32 v241, v154, v155
	v_add_f32_e32 v240, v173, v177
	v_add_f32_e32 v241, v130, v241
	v_add_f32_e32 v240, v165, v240
	v_add_f32_e32 v241, v131, v241
	v_add_f32_e32 v240, v166, v240
	v_add_f32_e32 v241, v128, v241
	s_waitcnt lgkmcnt(4)
	v_mfma_scale_f32_32x32x64_f8f6f4 v[84:99], v[68:75], v[100:107], v[216:231], v188, v247 op_sel_hi:[0,0,0]
	v_add_f32_e32 v240, v174, v240
	v_add_f32_e32 v241, v129, v241
	v_add_f32_e32 v240, v178, v240
	v_add_f32_e32 v241, v126, v241
	v_add_f32_e32 v240, v167, v240
	v_add_f32_e32 v241, v127, v241
	v_add_f32_e32 v240, v168, v240
	s_waitcnt lgkmcnt(2)
	v_mfma_scale_f32_32x32x64_f8f6f4 v[84:99], v[208:215], v[108:115], v[84:99], v188, v247 op_sel_hi:[0,0,0]
	v_add_f32_e32 v241, v124, v241
	v_add_f32_e32 v240, v175, v240
	v_add_f32_e32 v241, v125, v241
	v_add_f32_e32 v240, v179, v240
	v_add_f32_e32 v241, v160, v241
	v_add_f32_e32 v240, v169, v240
	v_add_f32_e32 v241, v161, v241
	s_waitcnt lgkmcnt(0)
	v_mfma_scale_f32_32x32x64_f8f6f4 v[68:83], v[200:207], v[100:107], v[216:231], v188, v247 op_sel_hi:[0,0,0]
	ds_read_b128 v[200:203], v194 offset:61440
	ds_read_b128 v[204:207], v195 offset:61440
	v_add_f32_e32 v240, v170, v240
	v_add_f32_e32 v241, v158, v241
	v_add_f32_e32 v240, v176, v240
	v_add_f32_e32 v241, v159, v241
	v_add_f32_e32 v240, v180, v240
	v_add_f32_e32 v241, v156, v241
	v_add_f32_e32 v240, v171, v240
	v_add_f32_e32 v241, v157, v241
	s_waitcnt lgkmcnt(0)
	v_mfma_scale_f32_32x32x64_f8f6f4 v[68:83], v[200:207], v[108:115], v[68:83], v188, v247 op_sel_hi:[0,0,0]
	v_add_f32_e32 v240, v172, v240
	v_add_f32_e32 v162, v240, v241
	v_mov_b32_e32 v163, v162
	s_nop 0
	s_nop 0
	v_permlane32_swap_b32_e32 v162, v163
	v_add_f32_e32 v162, v162, v163
	v_cmp_ge_f32_e32 vcc, 0x43c80000, v162
	s_cmp_eq_u64 vcc, exec
	s_cbranch_scc1 .Lring_norare_a1
	s_nop 15
	s_nop 15
	v_max3_f32 v240, v173, v177, v165
	v_max3_f32 v240, v240, v166, v174
	v_max3_f32 v240, v240, v178, v167
	v_max3_f32 v240, v240, v168, v175
	v_max3_f32 v240, v240, v179, v169
	v_max3_f32 v240, v240, v170, v176
	v_max3_f32 v240, v240, v180, v171
	v_max3_f32 v240, v240, v172, v154
	v_max3_f32 v240, v240, v155, v130
	v_max3_f32 v240, v240, v131, v128
	v_max3_f32 v240, v240, v129, v126
	v_max3_f32 v240, v240, v127, v124
	v_max3_f32 v240, v240, v125, v160
	v_max3_f32 v240, v240, v161, v158
	v_max3_f32 v240, v240, v159, v156
	v_max_f32_e32 v240, v240, v157
	v_mov_b32_e32 v241, v240
	s_nop 1
	v_permlane32_swap_b32_e32 v240, v241
	v_max_f32_e32 v240, v240, v241
	v_log_f32_e32 v249, v240
	s_nop 0
	v_ceil_f32_e32 v249, v249
	v_max_f32_e32 v249, 0, v249
	v_exp_f32_e64 v252, -v249
	s_nop 0
	v_fmamk_f32 v153, v249, 0x41000000, v153
	v_mul_f32_e32 v173, v173, v252
	v_mul_f32_e32 v177, v177, v252
	v_mul_f32_e32 v165, v165, v252
	v_mul_f32_e32 v166, v166, v252
	v_mul_f32_e32 v174, v174, v252
	v_mul_f32_e32 v178, v178, v252
	v_mul_f32_e32 v167, v167, v252
	v_mul_f32_e32 v168, v168, v252
	v_mul_f32_e32 v175, v175, v252
	v_mul_f32_e32 v179, v179, v252
	v_mul_f32_e32 v169, v169, v252
	v_mul_f32_e32 v170, v170, v252
	v_mul_f32_e32 v176, v176, v252
	v_mul_f32_e32 v180, v180, v252
	v_mul_f32_e32 v171, v171, v252
	v_mul_f32_e32 v172, v172, v252
	v_mul_f32_e32 v154, v154, v252
	v_mul_f32_e32 v155, v155, v252
	v_mul_f32_e32 v130, v130, v252
	v_mul_f32_e32 v131, v131, v252
	v_mul_f32_e32 v128, v128, v252
	v_mul_f32_e32 v129, v129, v252
	v_mul_f32_e32 v126, v126, v252
	v_mul_f32_e32 v127, v127, v252
	v_mul_f32_e32 v124, v124, v252
	v_mul_f32_e32 v125, v125, v252
	v_mul_f32_e32 v160, v160, v252
	v_mul_f32_e32 v161, v161, v252
	v_mul_f32_e32 v158, v158, v252
	v_mul_f32_e32 v159, v159, v252
	v_mul_f32_e32 v156, v156, v252
	v_mul_f32_e32 v157, v157, v252
	v_mul_f32_e32 v162, v162, v252
	v_mul_f32_e32 v145, v145, v252
	v_sub_f32_e32 v84, v84, v249
	v_sub_f32_e32 v85, v85, v249
	v_sub_f32_e32 v86, v86, v249
	v_sub_f32_e32 v87, v87, v249
	v_sub_f32_e32 v88, v88, v249
	v_sub_f32_e32 v89, v89, v249
	v_sub_f32_e32 v90, v90, v249
	v_sub_f32_e32 v91, v91, v249
	v_sub_f32_e32 v92, v92, v249
	v_sub_f32_e32 v93, v93, v249
	v_sub_f32_e32 v94, v94, v249
	v_sub_f32_e32 v95, v95, v249
	v_sub_f32_e32 v96, v96, v249
	v_sub_f32_e32 v97, v97, v249
	v_sub_f32_e32 v98, v98, v249
	v_sub_f32_e32 v99, v99, v249
	v_sub_f32_e32 v68, v68, v249
	v_sub_f32_e32 v69, v69, v249
	v_sub_f32_e32 v70, v70, v249
	v_sub_f32_e32 v71, v71, v249
	v_sub_f32_e32 v72, v72, v249
	v_sub_f32_e32 v73, v73, v249
	v_sub_f32_e32 v74, v74, v249
	v_sub_f32_e32 v75, v75, v249
	v_sub_f32_e32 v76, v76, v249
	v_sub_f32_e32 v77, v77, v249
	v_sub_f32_e32 v78, v78, v249
	v_sub_f32_e32 v79, v79, v249
	v_sub_f32_e32 v80, v80, v249
	v_sub_f32_e32 v81, v81, v249
	v_sub_f32_e32 v82, v82, v249
	v_sub_f32_e32 v83, v83, v249
	v_sub_f32_e32 v216, v216, v249
	v_sub_f32_e32 v217, v217, v249
	v_sub_f32_e32 v218, v218, v249
	v_sub_f32_e32 v219, v219, v249
	v_sub_f32_e32 v220, v220, v249
	v_sub_f32_e32 v221, v221, v249
	v_sub_f32_e32 v222, v222, v249
	v_sub_f32_e32 v223, v223, v249
	v_sub_f32_e32 v224, v224, v249
	v_sub_f32_e32 v225, v225, v249
	v_sub_f32_e32 v226, v226, v249
	v_sub_f32_e32 v227, v227, v249
	v_sub_f32_e32 v228, v228, v249
	v_sub_f32_e32 v229, v229, v249
	v_sub_f32_e32 v230, v230, v249
	v_sub_f32_e32 v231, v231, v249
	s_and_saveexec_b64 s[8:9], s[6:7]
	ds_write_b32 v184, v252 offset:128
	s_or_b64 exec, exec, s[8:9]
	s_waitcnt lgkmcnt(0)
	v_add_u32_e32 v253, v135, v185
	ds_read_b128 v[212:215], v253 offset:224
	ds_read_b128 v[208:211], v253 offset:192
	ds_read_b128 v[204:207], v253 offset:160
	ds_read_b128 v[200:203], v253 offset:128
	s_waitcnt lgkmcnt(0)
	v_pk_mul_f32 v[52:53], v[52:53], v[200:201]
	v_pk_mul_f32 v[54:55], v[54:55], v[202:203]
	v_pk_mul_f32 v[56:57], v[56:57], v[204:205]
	v_pk_mul_f32 v[58:59], v[58:59], v[206:207]
	v_pk_mul_f32 v[60:61], v[60:61], v[208:209]
	v_pk_mul_f32 v[62:63], v[62:63], v[210:211]
	v_pk_mul_f32 v[64:65], v[64:65], v[212:213]
	v_pk_mul_f32 v[66:67], v[66:67], v[214:215]
	v_pk_mul_f32 v[36:37], v[36:37], v[200:201]
	v_pk_mul_f32 v[38:39], v[38:39], v[202:203]
	v_pk_mul_f32 v[40:41], v[40:41], v[204:205]
	v_pk_mul_f32 v[42:43], v[42:43], v[206:207]
	v_pk_mul_f32 v[44:45], v[44:45], v[208:209]
	v_pk_mul_f32 v[46:47], v[46:47], v[210:211]
	v_pk_mul_f32 v[48:49], v[48:49], v[212:213]
	v_pk_mul_f32 v[50:51], v[50:51], v[214:215]
	v_pk_mul_f32 v[20:21], v[20:21], v[200:201]
	v_pk_mul_f32 v[22:23], v[22:23], v[202:203]
	v_pk_mul_f32 v[24:25], v[24:25], v[204:205]
	v_pk_mul_f32 v[26:27], v[26:27], v[206:207]
	v_pk_mul_f32 v[28:29], v[28:29], v[208:209]
	v_pk_mul_f32 v[30:31], v[30:31], v[210:211]
	v_pk_mul_f32 v[32:33], v[32:33], v[212:213]
	v_pk_mul_f32 v[34:35], v[34:35], v[214:215]
	v_pk_mul_f32 v[4:5], v[4:5], v[200:201]
	v_pk_mul_f32 v[6:7], v[6:7], v[202:203]
	v_pk_mul_f32 v[8:9], v[8:9], v[204:205]
	v_pk_mul_f32 v[10:11], v[10:11], v[206:207]
	v_pk_mul_f32 v[12:13], v[12:13], v[208:209]
	v_pk_mul_f32 v[14:15], v[14:15], v[210:211]
	v_pk_mul_f32 v[16:17], v[16:17], v[212:213]
	v_pk_mul_f32 v[18:19], v[18:19], v[214:215]
.Lring_norare_a1:
	ds_read_b128 v[200:203], v197 offset:8192
	ds_read_b128 v[204:207], v198 offset:8192
	ds_read_b128 v[208:211], v197 offset:10240
	ds_read_b128 v[212:215], v198 offset:10240
	v_add_u32_e32 v252, 0xffffe000, v152
	v_mov_b32_e32 v253, v3
	v_lshl_add_u64 v[252:253], v[148:149], 0, v[252:253]
	v_add_f32_e32 v145, v145, v162
	v_cvt_pk_fp8_f32 v232, v173, v177
	v_cvt_pk_fp8_f32 v233, v174, v178
	v_cvt_pk_fp8_f32 v234, v175, v179
	v_cvt_pk_fp8_f32 v235, v176, v180
	v_cvt_pk_fp8_f32 v232, v165, v166 op_sel:[0,0,1]
	v_cvt_pk_fp8_f32 v233, v167, v168 op_sel:[0,0,1]
	v_cvt_pk_fp8_f32 v234, v169, v170 op_sel:[0,0,1]
	v_cvt_pk_fp8_f32 v235, v171, v172 op_sel:[0,0,1]
	v_cvt_pk_fp8_f32 v236, v154, v155
	v_cvt_pk_fp8_f32 v237, v128, v129
	v_cvt_pk_fp8_f32 v238, v124, v125
	v_cvt_pk_fp8_f32 v239, v158, v159
	v_cvt_pk_fp8_f32 v236, v130, v131 op_sel:[0,0,1]
	v_cvt_pk_fp8_f32 v237, v126, v127 op_sel:[0,0,1]
	global_load_dwordx4 v[124:127], v[150:151], off offset:-64
	global_load_dwordx4 v[128:131], v[252:253], off
	s_waitcnt lgkmcnt(2)
	v_cvt_pk_fp8_f32 v238, v160, v161 op_sel:[0,0,1]
	v_cvt_pk_fp8_f32 v239, v156, v157 op_sel:[0,0,1]
	s_nop 0
	s_nop 0
	v_mfma_scale_f32_32x32x64_f8f6f4 v[52:67], v[232:239], v[200:207], v[52:67], v188, v188 op_sel_hi:[0,0,0]
	v_exp_f32_e32 v165, v84
	v_exp_f32_e32 v169, v85
	v_exp_f32_e32 v2, v86
	v_exp_f32_e32 v155, v87
	v_exp_f32_e32 v166, v88
	v_exp_f32_e32 v170, v89
	v_exp_f32_e32 v156, v90
	v_exp_f32_e32 v157, v91
	s_waitcnt lgkmcnt(0)
	v_mfma_scale_f32_32x32x64_f8f6f4 v[36:51], v[232:239], v[208:215], v[36:51], v188, v188 op_sel_hi:[0,0,0]
	ds_read_b128 v[200:203], v197 offset:12288
	ds_read_b128 v[204:207], v198 offset:12288
	ds_read_b128 v[208:211], v197 offset:14336
	ds_read_b128 v[212:215], v198 offset:14336
	v_exp_f32_e32 v167, v92
	v_exp_f32_e32 v171, v93
	v_exp_f32_e32 v158, v94
	v_exp_f32_e32 v159, v95
	v_exp_f32_e32 v168, v96
	v_exp_f32_e32 v172, v97
	v_exp_f32_e32 v160, v98
	v_exp_f32_e32 v161, v99
	s_waitcnt lgkmcnt(2)
	v_mfma_scale_f32_32x32x64_f8f6f4 v[20:35], v[232:239], v[200:207], v[20:35], v188, v188 op_sel_hi:[0,0,0]
	v_exp_f32_e32 v173, v68
	v_exp_f32_e32 v174, v69
	v_exp_f32_e32 v175, v70
	v_exp_f32_e32 v176, v71
	v_exp_f32_e32 v177, v72
	v_exp_f32_e32 v178, v73
	v_exp_f32_e32 v179, v74
	v_exp_f32_e32 v180, v75
	s_waitcnt lgkmcnt(0)
	v_mfma_scale_f32_32x32x64_f8f6f4 v[4:19], v[232:239], v[208:215], v[4:19], v188, v188 op_sel_hi:[0,0,0]
	v_exp_f32_e32 v181, v76
	v_exp_f32_e32 v182, v77
	v_exp_f32_e32 v183, v78
	v_exp_f32_e32 v246, v79
	v_exp_f32_e32 v248, v80
	v_exp_f32_e32 v250, v81
	v_exp_f32_e32 v251, v82
	v_exp_f32_e32 v164, v83
	s_waitcnt lgkmcnt(0)
	s_barrier
	s_waitcnt vmcnt(0)
	v_mov_b32_e32 v254, v124
	v_mov_b32_e32 v255, v126
	ds_write_b64 v189, v[254:255] offset:16384
	v_mov_b32_e32 v244, v125
	v_mov_b32_e32 v245, v127
	ds_write_b64 v190, v[244:245] offset:16384
	ds_write_b128 v191, v[128:131] offset:49152
	s_cmp_gt_u32 s15, 60
	s_cselect_b64 s[8:9], -1, 0
	s_and_b64 vcc, exec, s[8:9]
	s_cbranch_vccnz .Lring_noload_b1
	v_mov_b32_e32 v252, v152
	v_mov_b32_e32 v253, v3
	v_lshl_add_u64 v[120:121], v[148:149], 0, v[252:253]
	global_load_dwordx4 v[116:119], v[150:151], off
	s_nop 0
	global_load_dwordx4 v[120:123], v[120:121], off
.Lring_noload_b1:
	ds_read_b128 v[68:71], v192 offset:32768
	ds_read_b128 v[72:75], v193 offset:32768
	ds_read_b128 v[208:211], v194 offset:32768
	ds_read_b128 v[212:215], v195 offset:32768
	ds_read_b128 v[200:203], v192 offset:36864
	ds_read_b128 v[204:207], v193 offset:36864
	v_add_f32_e32 v241, v173, v174
	v_add_f32_e32 v240, v165, v169
	v_add_f32_e32 v241, v175, v241
	v_add_f32_e32 v240, v2, v240
	v_add_f32_e32 v241, v176, v241
	v_add_f32_e32 v240, v155, v240
	v_add_f32_e32 v241, v177, v241
	s_waitcnt lgkmcnt(4)
	v_mfma_scale_f32_32x32x64_f8f6f4 v[84:99], v[68:75], v[100:107], v[216:231], v188, v247 op_sel_hi:[0,0,0]
	v_add_f32_e32 v240, v166, v240
	v_add_f32_e32 v241, v178, v241
	v_add_f32_e32 v240, v170, v240
	v_add_f32_e32 v241, v179, v241
	v_add_f32_e32 v240, v156, v240
	v_add_f32_e32 v241, v180, v241
	v_add_f32_e32 v240, v157, v240
	s_waitcnt lgkmcnt(2)
	v_mfma_scale_f32_32x32x64_f8f6f4 v[84:99], v[208:215], v[108:115], v[84:99], v188, v247 op_sel_hi:[0,0,0]
	v_add_f32_e32 v241, v181, v241
	v_add_f32_e32 v240, v167, v240
	v_add_f32_e32 v241, v182, v241
	v_add_f32_e32 v240, v171, v240
	v_add_f32_e32 v241, v183, v241
	v_add_f32_e32 v240, v158, v240
	v_add_f32_e32 v241, v246, v241
	s_waitcnt lgkmcnt(0)
	v_mfma_scale_f32_32x32x64_f8f6f4 v[68:83], v[200:207], v[100:107], v[216:231], v188, v247 op_sel_hi:[0,0,0]
	ds_read_b128 v[200:203], v194 offset:36864
	ds_read_b128 v[204:207], v195 offset:36864
	v_add_f32_e32 v240, v159, v240
	v_add_f32_e32 v241, v248, v241
	v_add_f32_e32 v240, v168, v240
	v_add_f32_e32 v241, v250, v241
	v_add_f32_e32 v240, v172, v240
	v_add_f32_e32 v241, v251, v241
	v_add_f32_e32 v240, v160, v240
	v_add_f32_e32 v241, v164, v241
	s_waitcnt lgkmcnt(0)
	v_mfma_scale_f32_32x32x64_f8f6f4 v[68:83], v[200:207], v[108:115], v[68:83], v188, v247 op_sel_hi:[0,0,0]
	v_add_f32_e32 v240, v161, v240
	v_add_f32_e32 v162, v240, v241
	v_mov_b32_e32 v163, v162
	s_nop 0
	s_nop 0
	v_permlane32_swap_b32_e32 v162, v163
	v_add_f32_e32 v162, v162, v163
	v_cmp_ge_f32_e32 vcc, 0x43c80000, v162
	s_cmp_eq_u64 vcc, exec
	s_cbranch_scc1 .Lring_norare_b1
	s_nop 15
	s_nop 15
	v_max3_f32 v240, v165, v169, v2
	v_max3_f32 v240, v240, v155, v166
	v_max3_f32 v240, v240, v170, v156
	v_max3_f32 v240, v240, v157, v167
	v_max3_f32 v240, v240, v171, v158
	v_max3_f32 v240, v240, v159, v168
	v_max3_f32 v240, v240, v172, v160
	v_max3_f32 v240, v240, v161, v173
	v_max3_f32 v240, v240, v174, v175
	v_max3_f32 v240, v240, v176, v177
	v_max3_f32 v240, v240, v178, v179
	v_max3_f32 v240, v240, v180, v181
	v_max3_f32 v240, v240, v182, v183
	v_max3_f32 v240, v240, v246, v248
	v_max3_f32 v240, v240, v250, v251
	v_max_f32_e32 v240, v240, v164
	v_mov_b32_e32 v241, v240
	s_nop 1
	v_permlane32_swap_b32_e32 v240, v241
	v_max_f32_e32 v240, v240, v241
	v_log_f32_e32 v249, v240
	s_nop 0
	v_ceil_f32_e32 v249, v249
	v_max_f32_e32 v249, 0, v249
	v_exp_f32_e64 v252, -v249
	s_nop 0
	v_fmamk_f32 v153, v249, 0x41000000, v153
	v_mul_f32_e32 v165, v165, v252
	v_mul_f32_e32 v169, v169, v252
	v_mul_f32_e32 v2, v2, v252
	v_mul_f32_e32 v155, v155, v252
	v_mul_f32_e32 v166, v166, v252
	v_mul_f32_e32 v170, v170, v252
	v_mul_f32_e32 v156, v156, v252
	v_mul_f32_e32 v157, v157, v252
	v_mul_f32_e32 v167, v167, v252
	v_mul_f32_e32 v171, v171, v252
	v_mul_f32_e32 v158, v158, v252
	v_mul_f32_e32 v159, v159, v252
	v_mul_f32_e32 v168, v168, v252
	v_mul_f32_e32 v172, v172, v252
	v_mul_f32_e32 v160, v160, v252
	v_mul_f32_e32 v161, v161, v252
	v_mul_f32_e32 v173, v173, v252
	v_mul_f32_e32 v174, v174, v252
	v_mul_f32_e32 v175, v175, v252
	v_mul_f32_e32 v176, v176, v252
	v_mul_f32_e32 v177, v177, v252
	v_mul_f32_e32 v178, v178, v252
	v_mul_f32_e32 v179, v179, v252
	v_mul_f32_e32 v180, v180, v252
	v_mul_f32_e32 v181, v181, v252
	v_mul_f32_e32 v182, v182, v252
	v_mul_f32_e32 v183, v183, v252
	v_mul_f32_e32 v246, v246, v252
	v_mul_f32_e32 v248, v248, v252
	v_mul_f32_e32 v250, v250, v252
	v_mul_f32_e32 v251, v251, v252
	v_mul_f32_e32 v164, v164, v252
	v_mul_f32_e32 v162, v162, v252
	v_mul_f32_e32 v145, v145, v252
	v_sub_f32_e32 v84, v84, v249
	v_sub_f32_e32 v85, v85, v249
	v_sub_f32_e32 v86, v86, v249
	v_sub_f32_e32 v87, v87, v249
	v_sub_f32_e32 v88, v88, v249
	v_sub_f32_e32 v89, v89, v249
	v_sub_f32_e32 v90, v90, v249
	v_sub_f32_e32 v91, v91, v249
	v_sub_f32_e32 v92, v92, v249
	v_sub_f32_e32 v93, v93, v249
	v_sub_f32_e32 v94, v94, v249
	v_sub_f32_e32 v95, v95, v249
	v_sub_f32_e32 v96, v96, v249
	v_sub_f32_e32 v97, v97, v249
	v_sub_f32_e32 v98, v98, v249
	v_sub_f32_e32 v99, v99, v249
	v_sub_f32_e32 v68, v68, v249
	v_sub_f32_e32 v69, v69, v249
	v_sub_f32_e32 v70, v70, v249
	v_sub_f32_e32 v71, v71, v249
	v_sub_f32_e32 v72, v72, v249
	v_sub_f32_e32 v73, v73, v249
	v_sub_f32_e32 v74, v74, v249
	v_sub_f32_e32 v75, v75, v249
	v_sub_f32_e32 v76, v76, v249
	v_sub_f32_e32 v77, v77, v249
	v_sub_f32_e32 v78, v78, v249
	v_sub_f32_e32 v79, v79, v249
	v_sub_f32_e32 v80, v80, v249
	v_sub_f32_e32 v81, v81, v249
	v_sub_f32_e32 v82, v82, v249
	v_sub_f32_e32 v83, v83, v249
	v_sub_f32_e32 v216, v216, v249
	v_sub_f32_e32 v217, v217, v249
	v_sub_f32_e32 v218, v218, v249
	v_sub_f32_e32 v219, v219, v249
	v_sub_f32_e32 v220, v220, v249
	v_sub_f32_e32 v221, v221, v249
	v_sub_f32_e32 v222, v222, v249
	v_sub_f32_e32 v223, v223, v249
	v_sub_f32_e32 v224, v224, v249
	v_sub_f32_e32 v225, v225, v249
	v_sub_f32_e32 v226, v226, v249
	v_sub_f32_e32 v227, v227, v249
	v_sub_f32_e32 v228, v228, v249
	v_sub_f32_e32 v229, v229, v249
	v_sub_f32_e32 v230, v230, v249
	v_sub_f32_e32 v231, v231, v249
	s_and_saveexec_b64 s[10:11], s[6:7]
	ds_write_b32 v184, v252 offset:128
	s_or_b64 exec, exec, s[10:11]
	s_waitcnt lgkmcnt(0)
	v_add_u32_e32 v253, v135, v185
	ds_read_b128 v[212:215], v253 offset:224
	ds_read_b128 v[208:211], v253 offset:192
	ds_read_b128 v[204:207], v253 offset:160
	ds_read_b128 v[200:203], v253 offset:128
	s_waitcnt lgkmcnt(0)
	v_pk_mul_f32 v[52:53], v[52:53], v[200:201]
	v_pk_mul_f32 v[54:55], v[54:55], v[202:203]
	v_pk_mul_f32 v[56:57], v[56:57], v[204:205]
	v_pk_mul_f32 v[58:59], v[58:59], v[206:207]
	v_pk_mul_f32 v[60:61], v[60:61], v[208:209]
	v_pk_mul_f32 v[62:63], v[62:63], v[210:211]
	v_pk_mul_f32 v[64:65], v[64:65], v[212:213]
	v_pk_mul_f32 v[66:67], v[66:67], v[214:215]
	v_pk_mul_f32 v[36:37], v[36:37], v[200:201]
	v_pk_mul_f32 v[38:39], v[38:39], v[202:203]
	v_pk_mul_f32 v[40:41], v[40:41], v[204:205]
	v_pk_mul_f32 v[42:43], v[42:43], v[206:207]
	v_pk_mul_f32 v[44:45], v[44:45], v[208:209]
	v_pk_mul_f32 v[46:47], v[46:47], v[210:211]
	v_pk_mul_f32 v[48:49], v[48:49], v[212:213]
	v_pk_mul_f32 v[50:51], v[50:51], v[214:215]
	v_pk_mul_f32 v[20:21], v[20:21], v[200:201]
	v_pk_mul_f32 v[22:23], v[22:23], v[202:203]
	v_pk_mul_f32 v[24:25], v[24:25], v[204:205]
	v_pk_mul_f32 v[26:27], v[26:27], v[206:207]
	v_pk_mul_f32 v[28:29], v[28:29], v[208:209]
	v_pk_mul_f32 v[30:31], v[30:31], v[210:211]
	v_pk_mul_f32 v[32:33], v[32:33], v[212:213]
	v_pk_mul_f32 v[34:35], v[34:35], v[214:215]
	v_pk_mul_f32 v[4:5], v[4:5], v[200:201]
	v_pk_mul_f32 v[6:7], v[6:7], v[202:203]
	v_pk_mul_f32 v[8:9], v[8:9], v[204:205]
	v_pk_mul_f32 v[10:11], v[10:11], v[206:207]
	v_pk_mul_f32 v[12:13], v[12:13], v[208:209]
	v_pk_mul_f32 v[14:15], v[14:15], v[210:211]
	v_pk_mul_f32 v[16:17], v[16:17], v[212:213]
	v_pk_mul_f32 v[18:19], v[18:19], v[214:215]
.Lring_norare_b1:
	ds_read_b128 v[200:203], v197 offset:24576
	ds_read_b128 v[204:207], v198 offset:24576
	ds_read_b128 v[208:211], v197 offset:26624
	ds_read_b128 v[212:215], v198 offset:26624
	v_add_f32_e32 v145, v145, v162
	v_cvt_pk_fp8_f32 v232, v165, v169
	v_cvt_pk_fp8_f32 v233, v166, v170
	v_cvt_pk_fp8_f32 v234, v167, v171
	v_cvt_pk_fp8_f32 v235, v168, v172
	v_cvt_pk_fp8_f32 v232, v2, v155 op_sel:[0,0,1]
	v_cvt_pk_fp8_f32 v233, v156, v157 op_sel:[0,0,1]
	v_cvt_pk_fp8_f32 v234, v158, v159 op_sel:[0,0,1]
	v_cvt_pk_fp8_f32 v235, v160, v161 op_sel:[0,0,1]
	v_cvt_pk_fp8_f32 v236, v173, v174
	s_waitcnt lgkmcnt(2)
	v_cvt_pk_fp8_f32 v237, v177, v178
	v_cvt_pk_fp8_f32 v238, v181, v182
	v_cvt_pk_fp8_f32 v239, v248, v250
	v_cvt_pk_fp8_f32 v236, v175, v176 op_sel:[0,0,1]
	v_cvt_pk_fp8_f32 v237, v179, v180 op_sel:[0,0,1]
	v_cvt_pk_fp8_f32 v238, v183, v246 op_sel:[0,0,1]
	v_cvt_pk_fp8_f32 v239, v251, v164 op_sel:[0,0,1]
	s_nop 0
	s_nop 0
	v_mfma_scale_f32_32x32x64_f8f6f4 v[52:67], v[232:239], v[200:207], v[52:67], v188, v188 op_sel_hi:[0,0,0]
	v_exp_f32_e32 v173, v84
	v_exp_f32_e32 v177, v85
	v_exp_f32_e32 v165, v86
	v_exp_f32_e32 v166, v87
	v_exp_f32_e32 v174, v88
	v_exp_f32_e32 v178, v89
	v_exp_f32_e32 v167, v90
	v_exp_f32_e32 v168, v91
	s_waitcnt lgkmcnt(0)
	v_mfma_scale_f32_32x32x64_f8f6f4 v[36:51], v[232:239], v[208:215], v[36:51], v188, v188 op_sel_hi:[0,0,0]
	ds_read_b128 v[200:203], v197 offset:28672
	ds_read_b128 v[204:207], v198 offset:28672
	ds_read_b128 v[208:211], v197 offset:30720
	ds_read_b128 v[212:215], v198 offset:30720
	v_exp_f32_e32 v175, v92
	v_exp_f32_e32 v179, v93
	v_exp_f32_e32 v169, v94
	v_exp_f32_e32 v170, v95
	v_exp_f32_e32 v176, v96
	v_exp_f32_e32 v180, v97
	v_exp_f32_e32 v171, v98
	v_exp_f32_e32 v172, v99
	s_waitcnt lgkmcnt(2)
	v_mfma_scale_f32_32x32x64_f8f6f4 v[20:35], v[232:239], v[200:207], v[20:35], v188, v188 op_sel_hi:[0,0,0]
	v_exp_f32_e32 v154, v68
	v_exp_f32_e32 v155, v69
	v_exp_f32_e32 v130, v70
	v_exp_f32_e32 v131, v71
	v_exp_f32_e32 v128, v72
	v_exp_f32_e32 v129, v73
	v_exp_f32_e32 v126, v74
	v_exp_f32_e32 v127, v75
	s_waitcnt lgkmcnt(0)
	v_mfma_scale_f32_32x32x64_f8f6f4 v[4:19], v[232:239], v[208:215], v[4:19], v188, v188 op_sel_hi:[0,0,0]
	v_exp_f32_e32 v124, v76
	v_exp_f32_e32 v125, v77
	v_exp_f32_e32 v160, v78
	v_exp_f32_e32 v161, v79
	v_exp_f32_e32 v158, v80
	v_exp_f32_e32 v159, v81
	v_exp_f32_e32 v156, v82
	v_exp_f32_e32 v157, v83
	s_add_i32 s15, s15, 2
	v_lshl_add_u64 v[150:151], v[150:151], 0, s[28:29]
	v_add_u32_e32 v152, 0x4000, v152
	s_and_b64 vcc, exec, s[8:9]
	s_waitcnt lgkmcnt(0)
	s_barrier
	s_cbranch_vccnz .LBB0_421
	s_branch .LBB0_409

.LBB0_425:
	v_cndmask_b32_e64 v103, v103, v153, s[4:5]
	v_mul_f32_e32 v103, 0xbe000000, v103
	v_fmamk_f32 v84, v84, 0x3e000000, v103
	v_fmamk_f32 v85, v85, 0x3e000000, v103
	v_fmamk_f32 v112, v96, 0x3e000000, v103
	v_fmamk_f32 v96, v77, 0x3e000000, v103
	v_exp_f32_e32 v77, v84
	v_fmamk_f32 v86, v86, 0x3e000000, v103
	v_exp_f32_e32 v84, v85
	v_fmamk_f32 v87, v87, 0x3e000000, v103
	v_fmamk_f32 v104, v88, 0x3e000000, v103
	v_fmamk_f32 v88, v69, 0x3e000000, v103
	v_exp_f32_e32 v69, v86
	v_fmamk_f32 v105, v89, 0x3e000000, v103
	v_fmamk_f32 v68, v68, 0x3e000000, v103
	v_fmamk_f32 v89, v70, 0x3e000000, v103
	v_exp_f32_e32 v70, v87
	v_fmamk_f32 v113, v97, 0x3e000000, v103
	v_fmamk_f32 v97, v78, 0x3e000000, v103
	v_exp_f32_e32 v78, v104
	v_exp_f32_e32 v104, v68
	v_add_f32_e32 v68, 0, v77
	v_fmamk_f32 v106, v90, 0x3e000000, v103
	v_exp_f32_e32 v85, v105
	v_add_f32_e32 v68, v84, v68
	v_fmamk_f32 v107, v91, 0x3e000000, v103
	v_fmamk_f32 v90, v71, 0x3e000000, v103
	v_exp_f32_e32 v71, v106
	v_add_f32_e32 v68, v69, v68
	v_fmamk_f32 v108, v92, 0x3e000000, v103
	v_fmamk_f32 v91, v72, 0x3e000000, v103
	v_exp_f32_e32 v72, v107
	v_add_f32_e32 v68, v70, v68
	v_fmamk_f32 v109, v93, 0x3e000000, v103
	v_fmamk_f32 v114, v98, 0x3e000000, v103
	v_fmamk_f32 v98, v79, 0x3e000000, v103
	v_exp_f32_e32 v79, v108
	v_add_f32_e32 v68, v78, v68
	v_fmamk_f32 v110, v94, 0x3e000000, v103
	v_exp_f32_e32 v86, v109
	v_add_f32_e32 v68, v85, v68
	v_fmamk_f32 v111, v95, 0x3e000000, v103
	v_fmamk_f32 v92, v73, 0x3e000000, v103
	v_exp_f32_e32 v73, v110
	v_add_f32_e32 v68, v71, v68
	v_fmamk_f32 v93, v74, 0x3e000000, v103
	v_exp_f32_e32 v74, v111
	v_add_f32_e32 v68, v72, v68
	v_fmamk_f32 v115, v99, 0x3e000000, v103
	v_fmamk_f32 v99, v80, 0x3e000000, v103
	v_exp_f32_e32 v80, v112
	v_add_f32_e32 v68, v79, v68
	v_exp_f32_e32 v87, v113
	v_add_f32_e32 v68, v86, v68
	v_fmamk_f32 v94, v75, 0x3e000000, v103
	v_exp_f32_e32 v75, v114
	v_add_f32_e32 v68, v73, v68
	v_fmamk_f32 v95, v76, 0x3e000000, v103
	v_exp_f32_e32 v76, v115
	v_add_f32_e32 v68, v74, v68
	v_add_f32_e32 v68, v80, v68
	v_exp_f32_e32 v88, v88
	v_add_f32_e32 v68, v87, v68
	v_exp_f32_e32 v105, v89
	v_add_f32_e32 v68, v75, v68
	v_exp_f32_e32 v90, v90
	v_add_f32_e32 v68, v76, v68
	v_exp_f32_e32 v89, v91
	v_add_f32_e32 v68, v104, v68
	v_exp_f32_e32 v91, v92
	v_add_f32_e32 v68, v88, v68
	v_exp_f32_e32 v92, v93
	v_add_f32_e32 v68, v105, v68
	v_exp_f32_e32 v93, v94
	v_add_f32_e32 v68, v90, v68
	v_exp_f32_e32 v94, v95
	v_add_f32_e32 v68, v89, v68
	v_exp_f32_e32 v95, v96
	v_add_f32_e32 v68, v91, v68
	v_exp_f32_e32 v96, v97
	v_add_f32_e32 v68, v92, v68
	v_exp_f32_e32 v97, v98
	v_add_f32_e32 v68, v93, v68
	v_fmamk_f32 v81, v81, 0x3e000000, v103
	v_exp_f32_e32 v98, v99
	v_add_f32_e32 v68, v94, v68
	v_fmamk_f32 v82, v82, 0x3e000000, v103
	v_exp_f32_e32 v81, v81
	v_add_f32_e32 v68, v95, v68
	v_fmac_f32_e32 v103, 0x3e000000, v83
	v_exp_f32_e32 v99, v82
	v_add_f32_e32 v68, v96, v68
	v_mov_b32_e32 v82, v3
	v_mov_b32_e32 v83, v3
	v_exp_f32_e32 v103, v103
	v_add_f32_e32 v68, v97, v68
	v_cvt_pk_fp8_f32 v82, v77, v84
	v_cvt_pk_fp8_f32 v83, v78, v85
	v_mov_b32_e32 v84, v3
	v_mov_b32_e32 v85, v3
	v_add_f32_e32 v68, v98, v68
	v_cvt_pk_fp8_f32 v84, v79, v86
	v_cvt_pk_fp8_f32 v85, v80, v87
	v_mov_b32_e32 v86, v3
	v_mov_b32_e32 v87, v3
	v_add_f32_e32 v68, v81, v68
	v_cvt_pk_fp8_f32 v86, v104, v88
	v_cvt_pk_fp8_f32 v87, v89, v91
	v_mov_b32_e32 v88, v3
	v_mov_b32_e32 v89, v3
	v_add_f32_e32 v68, v99, v68
	v_cvt_pk_fp8_f32 v88, v94, v95
	v_cvt_pk_fp8_f32 v89, v98, v81
	v_add_f32_e32 v68, v103, v68
	v_cvt_pk_fp8_f32 v82, v69, v70 op_sel:[0,0,1]
	v_mov_b32_e32 v69, v68
	s_nop 1
	v_permlane32_swap_b32_e32 v68, v69
	v_cvt_pk_fp8_f32 v83, v71, v72 op_sel:[0,0,1]
	v_cvt_pk_fp8_f32 v84, v73, v74 op_sel:[0,0,1]
	v_cvt_pk_fp8_f32 v85, v75, v76 op_sel:[0,0,1]
	v_cvt_pk_fp8_f32 v86, v105, v90 op_sel:[0,0,1]
	v_cvt_pk_fp8_f32 v87, v92, v93 op_sel:[0,0,1]
	v_cvt_pk_fp8_f32 v88, v96, v97 op_sel:[0,0,1]
	v_cvt_pk_fp8_f32 v89, v99, v103 op_sel:[0,0,1]
	ds_read_b128 v[70:73], v197 offset:24576
	ds_read_b128 v[90:93], v197 offset:26624
	ds_read_b128 v[74:77], v198 offset:24576
	ds_read_b128 v[94:97], v198 offset:26624
	ds_read_b128 v[104:107], v197 offset:28672
	ds_read_b128 v[112:115], v197 offset:30720
	ds_read_b128 v[108:111], v198 offset:28672
	ds_read_b128 v[116:119], v198 offset:30720
	s_waitcnt lgkmcnt(5)
	v_mfma_scale_f32_32x32x64_f8f6f4 v[52:67], v[82:89], v[70:77], v[52:67], v188, v188 op_sel_hi:[0,0,0]
	s_waitcnt lgkmcnt(4)
	v_mfma_scale_f32_32x32x64_f8f6f4 v[36:51], v[82:89], v[90:97], v[36:51], v188, v188 op_sel_hi:[0,0,0]
	s_waitcnt lgkmcnt(1)
	v_mfma_scale_f32_32x32x64_f8f6f4 v[20:35], v[82:89], v[104:111], v[20:35], v188, v188 op_sel_hi:[0,0,0]
	s_waitcnt lgkmcnt(0)
	v_mfma_scale_f32_32x32x64_f8f6f4 v[4:19], v[82:89], v[112:119], v[4:19], v188, v188 op_sel_hi:[0,0,0]
	s_nop 0
	s_nop 15
	s_nop 15
	s_and_saveexec_b64 s[4:5], s[6:7]
	s_cbranch_execz .LBB0_386
	v_add_f32_e32 v70, v100, v101
	v_add_f32_e32 v70, v145, v70
	v_add_f32_e32 v2, v68, v69
	v_fmac_f32_e32 v2, v70, v102
	ds_write_b32 v184, v2
	s_branch .LBB0_386
